# conv1 epilogue bias loads issued at start of last MFMA phase; c2pvq branch-free 8-way argmin merge; recfin hand-written fin epilogue
# baseline (speedup 1.0000x reference)
.LBB4_80:
	s_or_b64 exec, exec, s[0:1]
	s_lshl_b32 s6, s3, 2
	s_waitcnt lgkmcnt(0)
	s_barrier
	v_lshrrev_b32_e32 v186, 1, v0
	v_lshrrev_b32_e32 v187, 3, v0
	v_and_b32_e32 v186, 0x60, v186
	v_and_b32_e32 v187, 4, v187
	v_or_b32_e32 v186, v186, v187
	v_lshlrev_b32_e32 v186, 2, v186
	global_load_dwordx4 v[154:157], v186, s[14:15]
	global_load_dwordx4 v[158:161], v186, s[14:15] offset:32
	global_load_dwordx4 v[162:165], v186, s[14:15] offset:64
	global_load_dwordx4 v[166:169], v186, s[14:15] offset:96
	global_load_dwordx4 v[170:173], v186, s[14:15] offset:1024
	global_load_dwordx4 v[174:177], v186, s[14:15] offset:1056
	global_load_dwordx4 v[178:181], v186, s[14:15] offset:1088
	global_load_dwordx4 v[182:185], v186, s[14:15] offset:1120
	s_waitcnt vmcnt(20)
	ds_read_b128 v[138:141], v1 offset:10400
	s_waitcnt vmcnt(18)
	ds_read_b128 v[142:145], v1 offset:10416
	ds_read_b128 v[146:149], v1
	ds_read_b128 v[150:153], v1 offset:16
	s_waitcnt vmcnt(16) lgkmcnt(1)
	v_mfma_f32_32x32x16_f16 v[50:65], v[134:137], v[146:149], v[50:65]
	s_waitcnt lgkmcnt(0)
	v_mfma_f32_32x32x16_f16 v[50:65], v[130:133], v[150:153], v[50:65]
	v_mfma_f32_32x32x16_f16 v[50:65], v[130:133], v[146:149], v[50:65]
	ds_read_b128 v[146:149], v1 offset:20800
	ds_read_b128 v[150:153], v1 offset:20816
	v_mfma_f32_32x32x16_f16 v[34:49], v[134:137], v[138:141], v[34:49]
	v_mfma_f32_32x32x16_f16 v[34:49], v[130:133], v[142:145], v[34:49]
	v_mfma_f32_32x32x16_f16 v[34:49], v[130:133], v[138:141], v[34:49]
	ds_read_b128 v[138:141], v1 offset:31200
	ds_read_b128 v[142:145], v1 offset:31216
	s_waitcnt lgkmcnt(3)
	v_mfma_f32_32x32x16_f16 v[18:33], v[134:137], v[146:149], v[18:33]
	s_waitcnt lgkmcnt(2)
	v_mfma_f32_32x32x16_f16 v[18:33], v[130:133], v[150:153], v[18:33]
	v_mfma_f32_32x32x16_f16 v[18:33], v[130:133], v[146:149], v[18:33]
	ds_read_b128 v[146:149], v1 offset:2640
	ds_read_b128 v[150:153], v1 offset:2656
	s_waitcnt lgkmcnt(3)
	v_mfma_f32_32x32x16_f16 v[2:17], v[134:137], v[138:141], v[2:17]
	s_waitcnt lgkmcnt(2)
	v_mfma_f32_32x32x16_f16 v[2:17], v[130:133], v[142:145], v[2:17]
	v_mfma_f32_32x32x16_f16 v[2:17], v[130:133], v[138:141], v[2:17]
	ds_read_b128 v[130:133], v1 offset:13040
	ds_read_b128 v[134:137], v1 offset:13056
	s_waitcnt vmcnt(14) lgkmcnt(3)
	v_mfma_f32_32x32x16_f16 v[50:65], v[126:129], v[146:149], v[50:65]
	s_waitcnt lgkmcnt(2)
	v_mfma_f32_32x32x16_f16 v[50:65], v[122:125], v[150:153], v[50:65]
	v_mfma_f32_32x32x16_f16 v[50:65], v[122:125], v[146:149], v[50:65]
	ds_read_b128 v[138:141], v1 offset:23440
	ds_read_b128 v[142:145], v1 offset:23456
	s_waitcnt lgkmcnt(3)
	v_mfma_f32_32x32x16_f16 v[34:49], v[126:129], v[130:133], v[34:49]
	s_waitcnt lgkmcnt(2)
	v_mfma_f32_32x32x16_f16 v[34:49], v[122:125], v[134:137], v[34:49]
	v_mfma_f32_32x32x16_f16 v[34:49], v[122:125], v[130:133], v[34:49]
	ds_read_b128 v[130:133], v1 offset:33840
	ds_read_b128 v[134:137], v1 offset:33856
	s_waitcnt lgkmcnt(3)
	v_mfma_f32_32x32x16_f16 v[18:33], v[126:129], v[138:141], v[18:33]
	s_waitcnt lgkmcnt(2)
	v_mfma_f32_32x32x16_f16 v[18:33], v[122:125], v[142:145], v[18:33]
	v_mfma_f32_32x32x16_f16 v[18:33], v[122:125], v[138:141], v[18:33]
	ds_read_b128 v[138:141], v1 offset:80
	ds_read_b128 v[142:145], v1 offset:96
	s_waitcnt lgkmcnt(3)
	v_mfma_f32_32x32x16_f16 v[2:17], v[126:129], v[130:133], v[2:17]
	s_waitcnt lgkmcnt(2)
	v_mfma_f32_32x32x16_f16 v[2:17], v[122:125], v[134:137], v[2:17]
	v_mfma_f32_32x32x16_f16 v[2:17], v[122:125], v[130:133], v[2:17]
	ds_read_b128 v[122:125], v1 offset:10480
	ds_read_b128 v[126:129], v1 offset:10496
	s_waitcnt vmcnt(12) lgkmcnt(3)
	v_mfma_f32_32x32x16_f16 v[50:65], v[118:121], v[138:141], v[50:65]
	s_waitcnt lgkmcnt(2)
	v_mfma_f32_32x32x16_f16 v[50:65], v[114:117], v[142:145], v[50:65]
	v_mfma_f32_32x32x16_f16 v[50:65], v[114:117], v[138:141], v[50:65]
	ds_read_b128 v[130:133], v1 offset:20880
	ds_read_b128 v[134:137], v1 offset:20896
	s_waitcnt lgkmcnt(3)
	v_mfma_f32_32x32x16_f16 v[34:49], v[118:121], v[122:125], v[34:49]
	s_waitcnt lgkmcnt(2)
	v_mfma_f32_32x32x16_f16 v[34:49], v[114:117], v[126:129], v[34:49]
	v_mfma_f32_32x32x16_f16 v[34:49], v[114:117], v[122:125], v[34:49]
	ds_read_b128 v[122:125], v1 offset:31280
	ds_read_b128 v[126:129], v1 offset:31296
	s_waitcnt lgkmcnt(3)
	v_mfma_f32_32x32x16_f16 v[18:33], v[118:121], v[130:133], v[18:33]
	s_waitcnt lgkmcnt(2)
	v_mfma_f32_32x32x16_f16 v[18:33], v[114:117], v[134:137], v[18:33]
	v_mfma_f32_32x32x16_f16 v[18:33], v[114:117], v[130:133], v[18:33]
	ds_read_b128 v[130:133], v1 offset:5200
	ds_read_b128 v[134:137], v1 offset:5216
	s_waitcnt lgkmcnt(3)
	v_mfma_f32_32x32x16_f16 v[2:17], v[118:121], v[122:125], v[2:17]
	s_waitcnt lgkmcnt(2)
	v_mfma_f32_32x32x16_f16 v[2:17], v[114:117], v[126:129], v[2:17]
	v_mfma_f32_32x32x16_f16 v[2:17], v[114:117], v[122:125], v[2:17]
	ds_read_b128 v[114:117], v1 offset:15600
	ds_read_b128 v[118:121], v1 offset:15616
	s_waitcnt vmcnt(10) lgkmcnt(3)
	v_mfma_f32_32x32x16_f16 v[50:65], v[110:113], v[130:133], v[50:65]
	s_waitcnt lgkmcnt(2)
	v_mfma_f32_32x32x16_f16 v[50:65], v[106:109], v[134:137], v[50:65]
	v_mfma_f32_32x32x16_f16 v[50:65], v[106:109], v[130:133], v[50:65]
	ds_read_b128 v[122:125], v1 offset:26000
	ds_read_b128 v[126:129], v1 offset:26016
	s_waitcnt lgkmcnt(3)
	v_mfma_f32_32x32x16_f16 v[34:49], v[110:113], v[114:117], v[34:49]
	s_waitcnt lgkmcnt(2)
	v_mfma_f32_32x32x16_f16 v[34:49], v[106:109], v[118:121], v[34:49]
	v_mfma_f32_32x32x16_f16 v[34:49], v[106:109], v[114:117], v[34:49]
	ds_read_b128 v[114:117], v1 offset:36400
	ds_read_b128 v[118:121], v1 offset:36416
	s_waitcnt lgkmcnt(3)
	v_mfma_f32_32x32x16_f16 v[18:33], v[110:113], v[122:125], v[18:33]
	s_waitcnt lgkmcnt(2)
	v_mfma_f32_32x32x16_f16 v[18:33], v[106:109], v[126:129], v[18:33]
	v_mfma_f32_32x32x16_f16 v[18:33], v[106:109], v[122:125], v[18:33]
	ds_read_b128 v[122:125], v1 offset:7840
	ds_read_b128 v[126:129], v1 offset:7856
	s_waitcnt lgkmcnt(3)
	v_mfma_f32_32x32x16_f16 v[2:17], v[110:113], v[114:117], v[2:17]
	s_waitcnt lgkmcnt(2)
	v_mfma_f32_32x32x16_f16 v[2:17], v[106:109], v[118:121], v[2:17]
	v_mfma_f32_32x32x16_f16 v[2:17], v[106:109], v[114:117], v[2:17]
	ds_read_b128 v[106:109], v1 offset:18240
	ds_read_b128 v[110:113], v1 offset:18256
	s_waitcnt vmcnt(8) lgkmcnt(3)
	v_mfma_f32_32x32x16_f16 v[50:65], v[102:105], v[122:125], v[50:65]
	s_waitcnt lgkmcnt(2)
	v_mfma_f32_32x32x16_f16 v[50:65], v[98:101], v[126:129], v[50:65]
	v_mfma_f32_32x32x16_f16 v[50:65], v[98:101], v[122:125], v[50:65]
	ds_read_b128 v[114:117], v1 offset:28640
	ds_read_b128 v[118:121], v1 offset:28656
	s_waitcnt lgkmcnt(3)
	v_mfma_f32_32x32x16_f16 v[34:49], v[102:105], v[106:109], v[34:49]
	s_waitcnt lgkmcnt(2)
	v_mfma_f32_32x32x16_f16 v[34:49], v[98:101], v[110:113], v[34:49]
	v_mfma_f32_32x32x16_f16 v[34:49], v[98:101], v[106:109], v[34:49]
	ds_read_b128 v[106:109], v1 offset:39040
	ds_read_b128 v[110:113], v1 offset:39056
	s_waitcnt lgkmcnt(3)
	v_mfma_f32_32x32x16_f16 v[18:33], v[102:105], v[114:117], v[18:33]
	s_waitcnt lgkmcnt(2)
	v_mfma_f32_32x32x16_f16 v[18:33], v[98:101], v[118:121], v[18:33]
	v_mfma_f32_32x32x16_f16 v[18:33], v[98:101], v[114:117], v[18:33]
	ds_read_b128 v[114:117], v1 offset:5280
	ds_read_b128 v[118:121], v1 offset:5296
	s_waitcnt lgkmcnt(3)
	v_mfma_f32_32x32x16_f16 v[2:17], v[102:105], v[106:109], v[2:17]
	s_waitcnt lgkmcnt(2)
	v_mfma_f32_32x32x16_f16 v[2:17], v[98:101], v[110:113], v[2:17]
	v_mfma_f32_32x32x16_f16 v[2:17], v[98:101], v[106:109], v[2:17]
	ds_read_b128 v[98:101], v1 offset:15680
	ds_read_b128 v[102:105], v1 offset:15696
	s_waitcnt vmcnt(6) lgkmcnt(3)
	v_mfma_f32_32x32x16_f16 v[50:65], v[94:97], v[114:117], v[50:65]
	s_waitcnt lgkmcnt(2)
	v_mfma_f32_32x32x16_f16 v[50:65], v[90:93], v[118:121], v[50:65]
	v_mfma_f32_32x32x16_f16 v[50:65], v[90:93], v[114:117], v[50:65]
	ds_read_b128 v[106:109], v1 offset:26080
	ds_read_b128 v[110:113], v1 offset:26096
	s_waitcnt lgkmcnt(3)
	v_mfma_f32_32x32x16_f16 v[34:49], v[94:97], v[98:101], v[34:49]
	s_waitcnt lgkmcnt(2)
	v_mfma_f32_32x32x16_f16 v[34:49], v[90:93], v[102:105], v[34:49]
	v_mfma_f32_32x32x16_f16 v[34:49], v[90:93], v[98:101], v[34:49]
	ds_read_b128 v[98:101], v1 offset:36480
	ds_read_b128 v[102:105], v1 offset:36496
	s_waitcnt lgkmcnt(3)
	v_mfma_f32_32x32x16_f16 v[18:33], v[94:97], v[106:109], v[18:33]
	s_waitcnt lgkmcnt(2)
	v_mfma_f32_32x32x16_f16 v[18:33], v[90:93], v[110:113], v[18:33]
	v_mfma_f32_32x32x16_f16 v[18:33], v[90:93], v[106:109], v[18:33]
	ds_read_b128 v[106:109], v1 offset:10400
	ds_read_b128 v[110:113], v1 offset:10416
	s_waitcnt lgkmcnt(3)
	v_mfma_f32_32x32x16_f16 v[2:17], v[94:97], v[98:101], v[2:17]
	s_waitcnt lgkmcnt(2)
	v_mfma_f32_32x32x16_f16 v[2:17], v[90:93], v[102:105], v[2:17]
	v_mfma_f32_32x32x16_f16 v[2:17], v[90:93], v[98:101], v[2:17]
	ds_read_b128 v[90:93], v1 offset:20800
	ds_read_b128 v[94:97], v1 offset:20816
	s_waitcnt vmcnt(4) lgkmcnt(3)
	v_mfma_f32_32x32x16_f16 v[50:65], v[86:89], v[106:109], v[50:65]
	s_waitcnt lgkmcnt(2)
	v_mfma_f32_32x32x16_f16 v[50:65], v[82:85], v[110:113], v[50:65]
	v_mfma_f32_32x32x16_f16 v[50:65], v[82:85], v[106:109], v[50:65]
	ds_read_b128 v[98:101], v1 offset:31200
	ds_read_b128 v[102:105], v1 offset:31216
	s_waitcnt lgkmcnt(3)
	v_mfma_f32_32x32x16_f16 v[34:49], v[86:89], v[90:93], v[34:49]
	s_waitcnt lgkmcnt(2)
	v_mfma_f32_32x32x16_f16 v[34:49], v[82:85], v[94:97], v[34:49]
	v_mfma_f32_32x32x16_f16 v[34:49], v[82:85], v[90:93], v[34:49]
	ds_read_b128 v[90:93], v1 offset:41600
	ds_read_b128 v[94:97], v1 offset:41616
	s_waitcnt lgkmcnt(3)
	v_mfma_f32_32x32x16_f16 v[18:33], v[86:89], v[98:101], v[18:33]
	s_waitcnt lgkmcnt(2)
	v_mfma_f32_32x32x16_f16 v[18:33], v[82:85], v[102:105], v[18:33]
	v_mfma_f32_32x32x16_f16 v[18:33], v[82:85], v[98:101], v[18:33]
	ds_read_b128 v[98:101], v1 offset:13040
	ds_read_b128 v[102:105], v1 offset:13056
	s_waitcnt lgkmcnt(3)
	v_mfma_f32_32x32x16_f16 v[2:17], v[86:89], v[90:93], v[2:17]
	s_waitcnt lgkmcnt(2)
	v_mfma_f32_32x32x16_f16 v[2:17], v[82:85], v[94:97], v[2:17]
	v_mfma_f32_32x32x16_f16 v[2:17], v[82:85], v[90:93], v[2:17]
	ds_read_b128 v[82:85], v1 offset:23440
	ds_read_b128 v[86:89], v1 offset:23456
	s_waitcnt vmcnt(2) lgkmcnt(3)
	v_mfma_f32_32x32x16_f16 v[50:65], v[78:81], v[98:101], v[50:65]
	s_waitcnt lgkmcnt(2)
	v_mfma_f32_32x32x16_f16 v[50:65], v[74:77], v[102:105], v[50:65]
	v_mfma_f32_32x32x16_f16 v[50:65], v[74:77], v[98:101], v[50:65]
	ds_read_b128 v[90:93], v1 offset:33840
	ds_read_b128 v[94:97], v1 offset:33856
	s_waitcnt lgkmcnt(3)
	v_mfma_f32_32x32x16_f16 v[34:49], v[78:81], v[82:85], v[34:49]
	s_waitcnt lgkmcnt(2)
	v_mfma_f32_32x32x16_f16 v[34:49], v[74:77], v[86:89], v[34:49]
	v_mfma_f32_32x32x16_f16 v[34:49], v[74:77], v[82:85], v[34:49]
	ds_read_b128 v[82:85], v1 offset:44240
	ds_read_b128 v[86:89], v1 offset:44256
	s_waitcnt lgkmcnt(3)
	v_mfma_f32_32x32x16_f16 v[18:33], v[78:81], v[90:93], v[18:33]
	s_waitcnt lgkmcnt(2)
	v_mfma_f32_32x32x16_f16 v[18:33], v[74:77], v[94:97], v[18:33]
	v_mfma_f32_32x32x16_f16 v[18:33], v[74:77], v[90:93], v[18:33]
	ds_read_b128 v[90:93], v1 offset:10480
	ds_read_b128 v[94:97], v1 offset:10496
	s_waitcnt lgkmcnt(3)
	v_mfma_f32_32x32x16_f16 v[2:17], v[78:81], v[82:85], v[2:17]
	s_waitcnt lgkmcnt(2)
	v_mfma_f32_32x32x16_f16 v[2:17], v[74:77], v[86:89], v[2:17]
	v_mfma_f32_32x32x16_f16 v[2:17], v[74:77], v[82:85], v[2:17]
	ds_read_b128 v[74:77], v1 offset:20880
	ds_read_b128 v[78:81], v1 offset:20896
	s_waitcnt vmcnt(0) lgkmcnt(3)
	v_mfma_f32_32x32x16_f16 v[50:65], v[70:73], v[90:93], v[50:65]
	s_waitcnt lgkmcnt(2)
	v_mfma_f32_32x32x16_f16 v[50:65], v[66:69], v[94:97], v[50:65]
	v_mfma_f32_32x32x16_f16 v[50:65], v[66:69], v[90:93], v[50:65]
	ds_read_b128 v[82:85], v1 offset:31280
	ds_read_b128 v[86:89], v1 offset:31296
	s_waitcnt lgkmcnt(3)
	v_mfma_f32_32x32x16_f16 v[34:49], v[70:73], v[74:77], v[34:49]
	s_waitcnt lgkmcnt(2)
	v_mfma_f32_32x32x16_f16 v[34:49], v[66:69], v[78:81], v[34:49]
	v_mfma_f32_32x32x16_f16 v[34:49], v[66:69], v[74:77], v[34:49]
	ds_read_b128 v[74:77], v1 offset:41680
	ds_read_b128 v[78:81], v1 offset:41696
	s_waitcnt lgkmcnt(3)
	v_mfma_f32_32x32x16_f16 v[18:33], v[70:73], v[82:85], v[18:33]
	s_waitcnt lgkmcnt(2)
	v_mfma_f32_32x32x16_f16 v[18:33], v[66:69], v[86:89], v[18:33]
	v_mfma_f32_32x32x16_f16 v[18:33], v[66:69], v[82:85], v[18:33]
	s_waitcnt lgkmcnt(1)
	v_mfma_f32_32x32x16_f16 v[2:17], v[70:73], v[74:77], v[2:17]
	s_waitcnt lgkmcnt(0)
	v_mfma_f32_32x32x16_f16 v[2:17], v[66:69], v[78:81], v[2:17]
	v_mfma_f32_32x32x16_f16 v[2:17], v[66:69], v[74:77], v[2:17]
	v_and_b32_e32 v151, 31, v0
	v_lshrrev_b32_e32 v66, 1, v0
	v_lshrrev_b32_e32 v67, 3, v0
	v_and_b32_e32 v66, 0x60, v66
	v_and_b32_e32 v67, 4, v67
	v_or_b32_e32 v66, v66, v67
	v_lshlrev_b32_e32 v66, 2, v66
	v_readfirstlane_b32 s24, v0
	v_lshlrev_b32_e32 v100, 5, v151
	v_lshl_add_u32 v100, v67, 2, v100
	v_lshl_or_b32 v101, s2, 5, v151
	v_cmp_eq_u32_e64 s[26:27], 0, v101
	s_lshr_b32 s24, s24, 6
	s_lshl_b32 s25, s4, 23
	s_lshl_b32 s24, s24, 21
	s_add_u32 s25, s25, s24
	s_lshl_b32 s24, s3, 14
	s_add_u32 s25, s25, s24
	s_lshl_b32 s24, s2, 10
	s_add_u32 s25, s25, s24
	s_add_u32 s22, s20, s25
	s_addc_u32 s23, s21, 0
	s_cmp_lg_u32 s3, 0
	s_cbranch_scc1 .Lc1e_inner
	global_load_dwordx4 v[118:121], v66, s[14:15] offset:512
	global_load_dwordx4 v[122:125], v66, s[14:15] offset:544
	global_load_dwordx4 v[126:129], v66, s[14:15] offset:576
	global_load_dwordx4 v[130:133], v66, s[14:15] offset:608
	global_load_dwordx4 v[134:137], v66, s[14:15] offset:1536
	global_load_dwordx4 v[138:141], v66, s[14:15] offset:1568
	global_load_dwordx4 v[142:145], v66, s[14:15] offset:1600
	global_load_dwordx4 v[146:149], v66, s[14:15] offset:1632
	s_waitcnt vmcnt(0)
	v_sub_f32_e32 v118, v154, v118
	v_sub_f32_e32 v150, v118, v170
	v_add_f32_e32 v150, v150, v134
	v_cndmask_b32_e64 v102, v118, v150, s[26:27]
	v_sub_f32_e32 v119, v155, v119
	v_sub_f32_e32 v150, v119, v171
	v_add_f32_e32 v150, v150, v135
	v_cndmask_b32_e64 v103, v119, v150, s[26:27]
	v_sub_f32_e32 v120, v156, v120
	v_sub_f32_e32 v150, v120, v172
	v_add_f32_e32 v150, v150, v136
	v_cndmask_b32_e64 v104, v120, v150, s[26:27]
	v_sub_f32_e32 v121, v157, v121
	v_sub_f32_e32 v150, v121, v173
	v_add_f32_e32 v150, v150, v137
	v_cndmask_b32_e64 v105, v121, v150, s[26:27]
	v_sub_f32_e32 v122, v158, v122
	v_sub_f32_e32 v150, v122, v174
	v_add_f32_e32 v150, v150, v138
	v_cndmask_b32_e64 v106, v122, v150, s[26:27]
	v_sub_f32_e32 v123, v159, v123
	v_sub_f32_e32 v150, v123, v175
	v_add_f32_e32 v150, v150, v139
	v_cndmask_b32_e64 v107, v123, v150, s[26:27]
	v_sub_f32_e32 v124, v160, v124
	v_sub_f32_e32 v150, v124, v176
	v_add_f32_e32 v150, v150, v140
	v_cndmask_b32_e64 v108, v124, v150, s[26:27]
	v_sub_f32_e32 v125, v161, v125
	v_sub_f32_e32 v150, v125, v177
	v_add_f32_e32 v150, v150, v141
	v_cndmask_b32_e64 v109, v125, v150, s[26:27]
	v_sub_f32_e32 v126, v162, v126
	v_sub_f32_e32 v150, v126, v178
	v_add_f32_e32 v150, v150, v142
	v_cndmask_b32_e64 v110, v126, v150, s[26:27]
	v_sub_f32_e32 v127, v163, v127
	v_sub_f32_e32 v150, v127, v179
	v_add_f32_e32 v150, v150, v143
	v_cndmask_b32_e64 v111, v127, v150, s[26:27]
	v_sub_f32_e32 v128, v164, v128
	v_sub_f32_e32 v150, v128, v180
	v_add_f32_e32 v150, v150, v144
	v_cndmask_b32_e64 v112, v128, v150, s[26:27]
	v_sub_f32_e32 v129, v165, v129
	v_sub_f32_e32 v150, v129, v181
	v_add_f32_e32 v150, v150, v145
	v_cndmask_b32_e64 v113, v129, v150, s[26:27]
	v_sub_f32_e32 v130, v166, v130
	v_sub_f32_e32 v150, v130, v182
	v_add_f32_e32 v150, v150, v146
	v_cndmask_b32_e64 v114, v130, v150, s[26:27]
	v_sub_f32_e32 v131, v167, v131
	v_sub_f32_e32 v150, v131, v183
	v_add_f32_e32 v150, v150, v147
	v_cndmask_b32_e64 v115, v131, v150, s[26:27]
	v_sub_f32_e32 v132, v168, v132
	v_sub_f32_e32 v150, v132, v184
	v_add_f32_e32 v150, v150, v148
	v_cndmask_b32_e64 v116, v132, v150, s[26:27]
	v_sub_f32_e32 v133, v169, v133
	v_sub_f32_e32 v150, v133, v185
	v_add_f32_e32 v150, v150, v149
	v_cndmask_b32_e64 v117, v133, v150, s[26:27]
	v_sub_f32_e32 v170, v154, v170
	v_cndmask_b32_e64 v170, v154, v170, s[26:27]
	v_sub_f32_e32 v171, v155, v171
	v_cndmask_b32_e64 v171, v155, v171, s[26:27]
	v_sub_f32_e32 v172, v156, v172
	v_cndmask_b32_e64 v172, v156, v172, s[26:27]
	v_sub_f32_e32 v173, v157, v173
	v_cndmask_b32_e64 v173, v157, v173, s[26:27]
	v_sub_f32_e32 v174, v158, v174
	v_cndmask_b32_e64 v174, v158, v174, s[26:27]
	v_sub_f32_e32 v175, v159, v175
	v_cndmask_b32_e64 v175, v159, v175, s[26:27]
	v_sub_f32_e32 v176, v160, v176
	v_cndmask_b32_e64 v176, v160, v176, s[26:27]
	v_sub_f32_e32 v177, v161, v177
	v_cndmask_b32_e64 v177, v161, v177, s[26:27]
	v_sub_f32_e32 v178, v162, v178
	v_cndmask_b32_e64 v178, v162, v178, s[26:27]
	v_sub_f32_e32 v179, v163, v179
	v_cndmask_b32_e64 v179, v163, v179, s[26:27]
	v_sub_f32_e32 v180, v164, v180
	v_cndmask_b32_e64 v180, v164, v180, s[26:27]
	v_sub_f32_e32 v181, v165, v181
	v_cndmask_b32_e64 v181, v165, v181, s[26:27]
	v_sub_f32_e32 v182, v166, v182
	v_cndmask_b32_e64 v182, v166, v182, s[26:27]
	v_sub_f32_e32 v183, v167, v183
	v_cndmask_b32_e64 v183, v167, v183, s[26:27]
	v_sub_f32_e32 v184, v168, v184
	v_cndmask_b32_e64 v184, v168, v184, s[26:27]
	v_sub_f32_e32 v185, v169, v185
	v_cndmask_b32_e64 v185, v169, v185, s[26:27]
	s_branch .Lc1e_store
.Lc1e_inner:
	s_waitcnt vmcnt(0)
	v_sub_f32_e32 v170, v154, v170
	v_cndmask_b32_e64 v170, v154, v170, s[26:27]
	v_mov_b32_e32 v102, v170
	v_sub_f32_e32 v171, v155, v171
	v_cndmask_b32_e64 v171, v155, v171, s[26:27]
	v_mov_b32_e32 v103, v171
	v_sub_f32_e32 v172, v156, v172
	v_cndmask_b32_e64 v172, v156, v172, s[26:27]
	v_mov_b32_e32 v104, v172
	v_sub_f32_e32 v173, v157, v173
	v_cndmask_b32_e64 v173, v157, v173, s[26:27]
	v_mov_b32_e32 v105, v173
	v_sub_f32_e32 v174, v158, v174
	v_cndmask_b32_e64 v174, v158, v174, s[26:27]
	v_mov_b32_e32 v106, v174
	v_sub_f32_e32 v175, v159, v175
	v_cndmask_b32_e64 v175, v159, v175, s[26:27]
	v_mov_b32_e32 v107, v175
	v_sub_f32_e32 v176, v160, v176
	v_cndmask_b32_e64 v176, v160, v176, s[26:27]
	v_mov_b32_e32 v108, v176
	v_sub_f32_e32 v177, v161, v177
	v_cndmask_b32_e64 v177, v161, v177, s[26:27]
	v_mov_b32_e32 v109, v177
	v_sub_f32_e32 v178, v162, v178
	v_cndmask_b32_e64 v178, v162, v178, s[26:27]
	v_mov_b32_e32 v110, v178
	v_sub_f32_e32 v179, v163, v179
	v_cndmask_b32_e64 v179, v163, v179, s[26:27]
	v_mov_b32_e32 v111, v179
	v_sub_f32_e32 v180, v164, v180
	v_cndmask_b32_e64 v180, v164, v180, s[26:27]
	v_mov_b32_e32 v112, v180
	v_sub_f32_e32 v181, v165, v181
	v_cndmask_b32_e64 v181, v165, v181, s[26:27]
	v_mov_b32_e32 v113, v181
	v_sub_f32_e32 v182, v166, v182
	v_cndmask_b32_e64 v182, v166, v182, s[26:27]
	v_mov_b32_e32 v114, v182
	v_sub_f32_e32 v183, v167, v183
	v_cndmask_b32_e64 v183, v167, v183, s[26:27]
	v_mov_b32_e32 v115, v183
	v_sub_f32_e32 v184, v168, v184
	v_cndmask_b32_e64 v184, v168, v184, s[26:27]
	v_mov_b32_e32 v116, v184
	v_sub_f32_e32 v185, v169, v185
	v_cndmask_b32_e64 v185, v169, v185, s[26:27]
	v_mov_b32_e32 v117, v185
.Lc1e_store:
	v_fmamk_f32 v50, v50, 0x3a800000, v102
	v_fmamk_f32 v51, v51, 0x3a800000, v103
	v_fmamk_f32 v52, v52, 0x3a800000, v104
	v_fmamk_f32 v53, v53, 0x3a800000, v105
	v_max_f32_e32 v50, 0, v50
	v_max_f32_e32 v51, 0, v51
	v_max_f32_e32 v52, 0, v52
	v_max_f32_e32 v53, 0, v53
	global_store_dwordx4 v100, v[50:53], s[22:23]
	s_add_u32 s22, s22, 0x1000
	s_addc_u32 s23, s23, 0
	v_fmamk_f32 v34, v34, 0x3a800000, v170
	v_fmamk_f32 v35, v35, 0x3a800000, v171
	v_fmamk_f32 v36, v36, 0x3a800000, v172
	v_fmamk_f32 v37, v37, 0x3a800000, v173
	v_max_f32_e32 v34, 0, v34
	v_max_f32_e32 v35, 0, v35
	v_max_f32_e32 v36, 0, v36
	v_max_f32_e32 v37, 0, v37
	global_store_dwordx4 v100, v[34:37], s[22:23]
	s_add_u32 s22, s22, 0x1000
	s_addc_u32 s23, s23, 0
	v_fmamk_f32 v18, v18, 0x3a800000, v170
	v_fmamk_f32 v19, v19, 0x3a800000, v171
	v_fmamk_f32 v20, v20, 0x3a800000, v172
	v_fmamk_f32 v21, v21, 0x3a800000, v173
	v_max_f32_e32 v18, 0, v18
	v_max_f32_e32 v19, 0, v19
	v_max_f32_e32 v20, 0, v20
	v_max_f32_e32 v21, 0, v21
	global_store_dwordx4 v100, v[18:21], s[22:23]
	s_add_u32 s22, s22, 0x1000
	s_addc_u32 s23, s23, 0
	v_fmamk_f32 v2, v2, 0x3a800000, v170
	v_fmamk_f32 v3, v3, 0x3a800000, v171
	v_fmamk_f32 v4, v4, 0x3a800000, v172
	v_fmamk_f32 v5, v5, 0x3a800000, v173
	v_max_f32_e32 v2, 0, v2
	v_max_f32_e32 v3, 0, v3
	v_max_f32_e32 v4, 0, v4
	v_max_f32_e32 v5, 0, v5
	global_store_dwordx4 v100, v[2:5], s[22:23]
	s_add_u32 s22, s22, 0x7d000
	s_addc_u32 s23, s23, 0
	v_fmamk_f32 v54, v54, 0x3a800000, v106
	v_fmamk_f32 v55, v55, 0x3a800000, v107
	v_fmamk_f32 v56, v56, 0x3a800000, v108
	v_fmamk_f32 v57, v57, 0x3a800000, v109
	v_max_f32_e32 v54, 0, v54
	v_max_f32_e32 v55, 0, v55
	v_max_f32_e32 v56, 0, v56
	v_max_f32_e32 v57, 0, v57
	global_store_dwordx4 v100, v[54:57], s[22:23]
	s_add_u32 s22, s22, 0x1000
	s_addc_u32 s23, s23, 0
	v_fmamk_f32 v38, v38, 0x3a800000, v174
	v_fmamk_f32 v39, v39, 0x3a800000, v175
	v_fmamk_f32 v40, v40, 0x3a800000, v176
	v_fmamk_f32 v41, v41, 0x3a800000, v177
	v_max_f32_e32 v38, 0, v38
	v_max_f32_e32 v39, 0, v39
	v_max_f32_e32 v40, 0, v40
	v_max_f32_e32 v41, 0, v41
	global_store_dwordx4 v100, v[38:41], s[22:23]
	s_add_u32 s22, s22, 0x1000
	s_addc_u32 s23, s23, 0
	v_fmamk_f32 v22, v22, 0x3a800000, v174
	v_fmamk_f32 v23, v23, 0x3a800000, v175
	v_fmamk_f32 v24, v24, 0x3a800000, v176
	v_fmamk_f32 v25, v25, 0x3a800000, v177
	v_max_f32_e32 v22, 0, v22
	v_max_f32_e32 v23, 0, v23
	v_max_f32_e32 v24, 0, v24
	v_max_f32_e32 v25, 0, v25
	global_store_dwordx4 v100, v[22:25], s[22:23]
	s_add_u32 s22, s22, 0x1000
	s_addc_u32 s23, s23, 0
	v_fmamk_f32 v6, v6, 0x3a800000, v174
	v_fmamk_f32 v7, v7, 0x3a800000, v175
	v_fmamk_f32 v8, v8, 0x3a800000, v176
	v_fmamk_f32 v9, v9, 0x3a800000, v177
	v_max_f32_e32 v6, 0, v6
	v_max_f32_e32 v7, 0, v7
	v_max_f32_e32 v8, 0, v8
	v_max_f32_e32 v9, 0, v9
	global_store_dwordx4 v100, v[6:9], s[22:23]
	s_add_u32 s22, s22, 0x7d000
	s_addc_u32 s23, s23, 0
	v_fmamk_f32 v58, v58, 0x3a800000, v110
	v_fmamk_f32 v59, v59, 0x3a800000, v111
	v_fmamk_f32 v60, v60, 0x3a800000, v112
	v_fmamk_f32 v61, v61, 0x3a800000, v113
	v_max_f32_e32 v58, 0, v58
	v_max_f32_e32 v59, 0, v59
	v_max_f32_e32 v60, 0, v60
	v_max_f32_e32 v61, 0, v61
	global_store_dwordx4 v100, v[58:61], s[22:23]
	s_add_u32 s22, s22, 0x1000
	s_addc_u32 s23, s23, 0
	v_fmamk_f32 v42, v42, 0x3a800000, v178
	v_fmamk_f32 v43, v43, 0x3a800000, v179
	v_fmamk_f32 v44, v44, 0x3a800000, v180
	v_fmamk_f32 v45, v45, 0x3a800000, v181
	v_max_f32_e32 v42, 0, v42
	v_max_f32_e32 v43, 0, v43
	v_max_f32_e32 v44, 0, v44
	v_max_f32_e32 v45, 0, v45
	global_store_dwordx4 v100, v[42:45], s[22:23]
	s_add_u32 s22, s22, 0x1000
	s_addc_u32 s23, s23, 0
	v_fmamk_f32 v26, v26, 0x3a800000, v178
	v_fmamk_f32 v27, v27, 0x3a800000, v179
	v_fmamk_f32 v28, v28, 0x3a800000, v180
	v_fmamk_f32 v29, v29, 0x3a800000, v181
	v_max_f32_e32 v26, 0, v26
	v_max_f32_e32 v27, 0, v27
	v_max_f32_e32 v28, 0, v28
	v_max_f32_e32 v29, 0, v29
	global_store_dwordx4 v100, v[26:29], s[22:23]
	s_add_u32 s22, s22, 0x1000
	s_addc_u32 s23, s23, 0
	v_fmamk_f32 v10, v10, 0x3a800000, v178
	v_fmamk_f32 v11, v11, 0x3a800000, v179
	v_fmamk_f32 v12, v12, 0x3a800000, v180
	v_fmamk_f32 v13, v13, 0x3a800000, v181
	v_max_f32_e32 v10, 0, v10
	v_max_f32_e32 v11, 0, v11
	v_max_f32_e32 v12, 0, v12
	v_max_f32_e32 v13, 0, v13
	global_store_dwordx4 v100, v[10:13], s[22:23]
	s_add_u32 s22, s22, 0x7d000
	s_addc_u32 s23, s23, 0
	v_fmamk_f32 v62, v62, 0x3a800000, v114
	v_fmamk_f32 v63, v63, 0x3a800000, v115
	v_fmamk_f32 v64, v64, 0x3a800000, v116
	v_fmamk_f32 v65, v65, 0x3a800000, v117
	v_max_f32_e32 v62, 0, v62
	v_max_f32_e32 v63, 0, v63
	v_max_f32_e32 v64, 0, v64
	v_max_f32_e32 v65, 0, v65
	global_store_dwordx4 v100, v[62:65], s[22:23]
	s_add_u32 s22, s22, 0x1000
	s_addc_u32 s23, s23, 0
	v_fmamk_f32 v46, v46, 0x3a800000, v182
	v_fmamk_f32 v47, v47, 0x3a800000, v183
	v_fmamk_f32 v48, v48, 0x3a800000, v184
	v_fmamk_f32 v49, v49, 0x3a800000, v185
	v_max_f32_e32 v46, 0, v46
	v_max_f32_e32 v47, 0, v47
	v_max_f32_e32 v48, 0, v48
	v_max_f32_e32 v49, 0, v49
	global_store_dwordx4 v100, v[46:49], s[22:23]
	s_add_u32 s22, s22, 0x1000
	s_addc_u32 s23, s23, 0
	v_fmamk_f32 v30, v30, 0x3a800000, v182
	v_fmamk_f32 v31, v31, 0x3a800000, v183
	v_fmamk_f32 v32, v32, 0x3a800000, v184
	v_fmamk_f32 v33, v33, 0x3a800000, v185
	v_max_f32_e32 v30, 0, v30
	v_max_f32_e32 v31, 0, v31
	v_max_f32_e32 v32, 0, v32
	v_max_f32_e32 v33, 0, v33
	global_store_dwordx4 v100, v[30:33], s[22:23]
	s_add_u32 s22, s22, 0x1000
	s_addc_u32 s23, s23, 0
	v_fmamk_f32 v14, v14, 0x3a800000, v182
	v_fmamk_f32 v15, v15, 0x3a800000, v183
	v_fmamk_f32 v16, v16, 0x3a800000, v184
	v_fmamk_f32 v17, v17, 0x3a800000, v185
	v_max_f32_e32 v14, 0, v14
	v_max_f32_e32 v15, 0, v15
	v_max_f32_e32 v16, 0, v16
	v_max_f32_e32 v17, 0, v17
	global_store_dwordx4 v100, v[14:17], s[22:23]
	s_endpgm
	.p2align	8

.LBB5_99:
	s_or_b64 exec, exec, s[6:7]
	s_movk_i32 s5, 0x7f
	s_lshl_b32 s15, s2, 5
	v_cmp_lt_u32_e32 vcc, s5, v0
	v_lshrrev_b32_e32 v2, 5, v0
	s_waitcnt lgkmcnt(0)
	s_barrier
	s_and_saveexec_b64 s[8:9], vcc
	s_xor_b64 s[8:9], exec, s[8:9]
	s_ashr_i32 s5, s4, 31
	s_lshl_b64 s[6:7], s[4:5], 12
	s_ashr_i32 s5, s15, 31
	s_add_u32 s6, s6, s15
	v_lshrrev_b32_e32 v2, 5, v0
	s_addc_u32 s7, s7, s5
	s_or_saveexec_b64 s[8:9], s[8:9]
	s_lshl_b32 s14, s3, 2
	v_mov_b64_e32 v[6:7], s[6:7]
	s_xor_b64 exec, exec, s[8:9]
	s_cbranch_execz .LBB5_131
	v_lshlrev_b32_e32 v5, 2, v0
	v_add_u32_e32 v6, 0x11000, v5
	v_add_u32_e32 v7, 0x12000, v5
	ds_read_b32 v212, v6
	ds_read_b32 v213, v7
	ds_read_b32 v214, v6 offset:512
	ds_read_b32 v215, v7 offset:512
	ds_read_b32 v216, v6 offset:1024
	ds_read_b32 v217, v7 offset:1024
	ds_read_b32 v218, v6 offset:1536
	ds_read_b32 v219, v7 offset:1536
	ds_read_b32 v220, v6 offset:2048
	ds_read_b32 v221, v7 offset:2048
	ds_read_b32 v222, v6 offset:2560
	ds_read_b32 v223, v7 offset:2560
	ds_read_b32 v224, v6 offset:3072
	ds_read_b32 v225, v7 offset:3072
	ds_read_b32 v226, v6 offset:3584
	ds_read_b32 v227, v7 offset:3584
	s_waitcnt lgkmcnt(0)
	v_mov_b32_e32 v4, v212
	v_mov_b32_e32 v3, v213
	v_cmp_lt_f32_e64 s[10:11], v214, v4
	v_cmp_eq_f32_e32 vcc, v214, v4
	v_cmp_lt_i32_e64 s[6:7], v215, v3
	s_and_b64 s[6:7], vcc, s[6:7]
	s_or_b64 s[10:11], s[10:11], s[6:7]
	v_cndmask_b32_e64 v4, v4, v214, s[10:11]
	v_cndmask_b32_e64 v3, v3, v215, s[10:11]
	v_cmp_lt_f32_e64 s[10:11], v216, v4
	v_cmp_eq_f32_e32 vcc, v216, v4
	v_cmp_lt_i32_e64 s[6:7], v217, v3
	s_and_b64 s[6:7], vcc, s[6:7]
	s_or_b64 s[10:11], s[10:11], s[6:7]
	v_cndmask_b32_e64 v4, v4, v216, s[10:11]
	v_cndmask_b32_e64 v3, v3, v217, s[10:11]
	v_cmp_lt_f32_e64 s[10:11], v218, v4
	v_cmp_eq_f32_e32 vcc, v218, v4
	v_cmp_lt_i32_e64 s[6:7], v219, v3
	s_and_b64 s[6:7], vcc, s[6:7]
	s_or_b64 s[10:11], s[10:11], s[6:7]
	v_cndmask_b32_e64 v4, v4, v218, s[10:11]
	v_cndmask_b32_e64 v3, v3, v219, s[10:11]
	v_cmp_lt_f32_e64 s[10:11], v220, v4
	v_cmp_eq_f32_e32 vcc, v220, v4
	v_cmp_lt_i32_e64 s[6:7], v221, v3
	s_and_b64 s[6:7], vcc, s[6:7]
	s_or_b64 s[10:11], s[10:11], s[6:7]
	v_cndmask_b32_e64 v4, v4, v220, s[10:11]
	v_cndmask_b32_e64 v3, v3, v221, s[10:11]
	v_cmp_lt_f32_e64 s[10:11], v222, v4
	v_cmp_eq_f32_e32 vcc, v222, v4
	v_cmp_lt_i32_e64 s[6:7], v223, v3
	s_and_b64 s[6:7], vcc, s[6:7]
	s_or_b64 s[10:11], s[10:11], s[6:7]
	v_cndmask_b32_e64 v4, v4, v222, s[10:11]
	v_cndmask_b32_e64 v3, v3, v223, s[10:11]
	v_cmp_lt_f32_e64 s[10:11], v224, v4
	v_cmp_eq_f32_e32 vcc, v224, v4
	v_cmp_lt_i32_e64 s[6:7], v225, v3
	s_and_b64 s[6:7], vcc, s[6:7]
	s_or_b64 s[10:11], s[10:11], s[6:7]
	v_cndmask_b32_e64 v4, v4, v224, s[10:11]
	v_cndmask_b32_e64 v3, v3, v225, s[10:11]
	v_cmp_lt_f32_e64 s[10:11], v226, v4
	v_cmp_eq_f32_e32 vcc, v226, v4
	v_cmp_lt_i32_e64 s[6:7], v227, v3
	s_and_b64 s[6:7], vcc, s[6:7]
	s_or_b64 s[10:11], s[10:11], s[6:7]
	v_cndmask_b32_e64 v4, v4, v226, s[10:11]
	v_cndmask_b32_e64 v3, v3, v227, s[10:11]
.LBB5_130:
	v_mov_b32_e32 v4, 0x13000
	s_ashr_i32 s5, s4, 31
	v_lshl_or_b32 v4, v0, 2, v4
	s_lshl_b64 s[6:7], s[4:5], 12
	s_ashr_i32 s5, s15, 31
	ds_write_b32 v4, v3
	v_or_b32_e32 v4, s14, v2
	s_add_u32 s6, s6, s15
	v_lshlrev_b32_e32 v4, 6, v4
	s_addc_u32 s7, s7, s5
	s_waitcnt lgkmcnt(1)
	v_ashrrev_i32_e32 v5, 31, v4
	v_or_b32_e32 v6, s6, v150
	v_mov_b32_e32 v7, s7
	v_cvt_f32_i32_e32 v8, v3
	v_lshl_add_u64 v[4:5], v[6:7], 0, v[4:5]
	v_lshlrev_b64 v[4:5], 2, v[4:5]
	v_lshl_add_u64 v[6:7], s[44:45], 0, v[4:5]
	global_store_dword v[6:7], v8, off
	v_lshl_add_u64 v[4:5], s[46:47], 0, v[4:5]
	v_mov_b64_e32 v[6:7], s[6:7]
	global_store_dword v[4:5], v3, off
